# split-K partials stored as [row][code] by K1 (dword stores) so K2 reads them fully coalesced (4x fewer cache-line requests)
# speedup vs baseline: 1.0469x; 1.0253x over previous
.Lep_skip:
	v_add_u32_e32 v40, s6, v194
	v_add_u32_e32 v41, s5, v40
	v_add_u32_e32 v42, s5, v41
	v_add_u32_e32 v43, s5, v42
	v_add_u32_e32 v44, s5, v43
	v_add_u32_e32 v45, s5, v44
	v_add_u32_e32 v46, s5, v45
	v_add_u32_e32 v47, s5, v46
	v_add_u32_e32 v66, 0xfc00, v194
	s_waitcnt lgkmcnt(0)
	s_nop 7
	ds_write_b128 v34, v[58:61]
	ds_write_b128 v36, v[62:65]
	ds_write_b128 v37, v[74:77]
	ds_write_b128 v38, v[78:81]
	ds_write_b128 v39, v[82:85]
	ds_write_b128 v48, v[86:89]
	ds_write_b128 v49, v[90:93]
	ds_write_b128 v50, v[94:97]
	ds_write_b128 v51, v[98:101]
	ds_write_b128 v35, v[102:105]
	ds_write_b128 v52, v[106:109]
	ds_write_b128 v53, v[110:113]
	ds_write_b128 v54, v[114:117]
	ds_write_b128 v55, v[118:121]
	ds_write_b128 v56, v[2:5]
	ds_write_b128 v57, v[6:9]
	s_waitcnt lgkmcnt(0)
	v_bfe_u32 v68, v0, 6, 1
	v_bfe_u32 v69, v0, 4, 2
	v_lshrrev_b32_e32 v70, 7, v0
	v_and_b32_e32 v71, 15, v0
	v_lshlrev_b32_e32 v68, 13, v68
	v_lshl_or_b32 v68, v69, 11, v68
	v_lshl_or_b32 v68, v70, 6, v68
	v_lshl_or_b32 v67, v71, 2, v68
	s_barrier
	ds_read_b128 v[2:5], v194
	ds_read_b128 v[6:9], v194 offset:9216
	ds_read_b128 v[10:13], v194 offset:18432
	ds_read_b128 v[14:17], v40
	ds_read_b128 v[18:21], v41
	s_nop 0
	s_lshl_b32 s2, s16, 3
	s_or_b32 s2, s2, s17
	s_waitcnt lgkmcnt(3)
	v_pk_add_f32 v[8:9], v[4:5], v[8:9]
	v_pk_add_f32 v[22:23], v[2:3], v[6:7]
	ds_read_b128 v[2:5], v42
	s_waitcnt lgkmcnt(3)
	v_pk_add_f32 v[26:27], v[8:9], v[12:13]
	ds_read_b128 v[6:9], v194 offset:27648
	v_pk_add_f32 v[28:29], v[22:23], v[10:11]
	ds_read_b128 v[10:13], v194 offset:36864
	ds_read_b128 v[22:25], v43
	s_nop 0
	s_ashr_i32 s3, s2, 31
	s_waitcnt lgkmcnt(2)
	v_pk_add_f32 v[26:27], v[26:27], v[8:9]
	v_pk_add_f32 v[28:29], v[28:29], v[6:7]
	ds_read_b128 v[6:9], v194 offset:46080
	s_nop 0
	s_waitcnt lgkmcnt(2)
	v_pk_add_f32 v[30:31], v[26:27], v[12:13]
	v_pk_add_f32 v[32:33], v[28:29], v[10:11]
	ds_read_b128 v[10:13], v194 offset:55296
	s_nop 0
	ds_read_b128 v[26:29], v66
	s_lshl_b64 s[2:3], s[2:3], 14
	s_waitcnt lgkmcnt(2)
	v_pk_add_f32 v[8:9], v[30:31], v[8:9]
	v_pk_add_f32 v[6:7], v[32:33], v[6:7]
	s_add_u32 s2, s12, s2
	s_waitcnt lgkmcnt(1)
	v_pk_add_f32 v[8:9], v[8:9], v[12:13]
	v_pk_add_f32 v[6:7], v[6:7], v[10:11]
	s_addc_u32 s3, s13, s3
	s_mov_b64 s[6:7], s[2:3]
	s_waitcnt lgkmcnt(0)
	v_pk_add_f32 v[8:9], v[8:9], v[28:29]
	v_pk_add_f32 v[6:7], v[6:7], v[26:27]
	global_store_dword v67, v6, s[2:3]
	global_store_dword v67, v7, s[2:3] offset:512
	global_store_dword v67, v8, s[2:3] offset:1024
	global_store_dword v67, v9, s[2:3] offset:1536
	s_nop 0
	v_lshl_add_u64 v[26:27], s[2:3], 0, v[194:195]
	v_pk_add_f32 v[6:7], v[16:17], v[20:21]
	v_pk_add_f32 v[8:9], v[14:15], v[18:19]
	v_pk_add_f32 v[6:7], v[6:7], v[4:5]
	v_pk_add_f32 v[8:9], v[8:9], v[2:3]
	ds_read_b128 v[2:5], v44
	s_nop 0
	v_pk_add_f32 v[10:11], v[6:7], v[24:25]
	v_pk_add_f32 v[12:13], v[8:9], v[22:23]
	ds_read_b128 v[6:9], v45
	s_nop 0
	s_waitcnt lgkmcnt(1)
	v_pk_add_f32 v[14:15], v[10:11], v[4:5]
	v_pk_add_f32 v[16:17], v[12:13], v[2:3]
	ds_read_b128 v[2:5], v46
	s_nop 0
	ds_read_b128 v[10:13], v47
	s_waitcnt lgkmcnt(2)
	v_pk_add_f32 v[6:7], v[16:17], v[6:7]
	v_pk_add_f32 v[8:9], v[14:15], v[8:9]
	s_waitcnt lgkmcnt(1)
	v_pk_add_f32 v[2:3], v[6:7], v[2:3]
	v_add_co_u32_e32 v6, vcc, 0x2000, v26
	v_pk_add_f32 v[4:5], v[8:9], v[4:5]
	s_nop 0
	v_addc_co_u32_e32 v7, vcc, 0, v27, vcc
	s_movk_i32 s2, 0x80
	s_waitcnt lgkmcnt(0)
	v_pk_add_f32 v[4:5], v[4:5], v[12:13]
	v_pk_add_f32 v[2:3], v[2:3], v[10:11]
	v_cmp_gt_u32_e32 vcc, s2, v0
	global_store_dword v67, v2, s[6:7] offset:256
	global_store_dword v67, v3, s[6:7] offset:768
	global_store_dword v67, v4, s[6:7] offset:1280
	global_store_dword v67, v5, s[6:7] offset:1792
	s_and_saveexec_b64 s[2:3], vcc
	s_cbranch_execz .LBB0_10
	v_lshlrev_b32_e32 v1, 2, v0
	v_or_b32_e32 v2, 0x20000, v1
	v_add_u32_e32 v3, 0x20200, v1
	v_add_u32_e32 v4, 0x20400, v1
	v_add_u32_e32 v5, 0x20600, v1
	v_or_b32_e32 v6, 0x20800, v1
	v_add_u32_e32 v7, 0x20a00, v1
	v_add_u32_e32 v8, 0x20c00, v1
	v_add_u32_e32 v9, 0x20e00, v1
	ds_read_b32 v2, v2
	ds_read_b32 v3, v3
	ds_read_b32 v4, v4
	ds_read_b32 v5, v5
	ds_read_b32 v6, v6
	ds_read_b32 v7, v7
	ds_read_b32 v8, v8
	ds_read_b32 v9, v9
	s_waitcnt lgkmcnt(7)
	v_add_f32_e32 v2, 0, v2
	s_waitcnt lgkmcnt(6)
	v_add_f32_e32 v2, v2, v3
	s_waitcnt lgkmcnt(5)
	v_add_f32_e32 v2, v2, v4
	s_waitcnt lgkmcnt(4)
	v_add_f32_e32 v2, v2, v5
	s_waitcnt lgkmcnt(3)
	v_add_f32_e32 v2, v2, v6
	s_waitcnt lgkmcnt(2)
	v_add_f32_e32 v2, v2, v7
	s_waitcnt lgkmcnt(1)
	v_add_f32_e32 v2, v2, v8
	s_waitcnt lgkmcnt(0)
	v_add_f32_e32 v2, v2, v9
	v_or_b32_e32 v3, 0x21000, v1
	v_add_u32_e32 v4, 0x21200, v1
	v_add_u32_e32 v5, 0x21400, v1
	v_add_u32_e32 v6, 0x21600, v1
	v_or_b32_e32 v7, 0x21800, v1
	v_add_u32_e32 v8, 0x21a00, v1
	v_add_u32_e32 v9, 0x21c00, v1
	v_add_u32_e32 v1, 0x21e00, v1
	ds_read_b32 v3, v3
	ds_read_b32 v4, v4
	ds_read_b32 v5, v5
	ds_read_b32 v6, v6
	ds_read_b32 v7, v7
	ds_read_b32 v8, v8
	ds_read_b32 v9, v9
	ds_read_b32 v1, v1
	s_waitcnt lgkmcnt(7)
	v_add_f32_e32 v2, v2, v3
	s_waitcnt lgkmcnt(6)
	v_add_f32_e32 v2, v2, v4
	s_waitcnt lgkmcnt(5)
	v_add_f32_e32 v2, v2, v5
	s_waitcnt lgkmcnt(0)
	v_add_f32_e32 v2, v2, v6
	v_add_f32_e32 v2, v2, v7
	s_lshl_b32 s2, s16, 10
	s_lshl_b32 s3, s17, 7
	v_add_f32_e32 v2, v2, v8
	s_or_b32 s2, s2, s3
	v_add_f32_e32 v2, v2, v9
	v_or_b32_e32 v0, s2, v0
	v_add_f32_e32 v2, v2, v1
	v_ashrrev_i32_e32 v1, 31, v0
	v_lshl_add_u64 v[0:1], v[0:1], 2, s[24:25]
	global_store_dword v[0:1], v2, off sc0 sc1

_Z9k2_reducePKfS0_S0_PdPiS1_:
	s_load_dwordx4 s[12:15], s[0:1], 0x0
	s_load_dwordx2 s[4:5], s[0:1], 0x10
	s_load_dwordx4 s[28:31], s[0:1], 0x18
	s_load_dwordx2 s[32:33], s[0:1], 0x28
	v_lshrrev_b32_e32 v1, 3, v0
	s_lshr_b32 s3, s2, 3
	s_lshr_b32 s7, s2, 7
	v_and_b32_e32 v2, 14, v1
	v_add_lshl_u32 v34, v2, s7, 6
	s_lshl_b32 s7, s3, 2
	s_and_b32 s6, s2, 7
	s_and_b32 s16, s7, 48
	s_waitcnt lgkmcnt(0)
	s_and_b32 s9, s15, 0xffff
	s_mov_b32 s8, s14
	s_mul_hi_u32 s14, s3, 0x1f400
	s_mul_i32 s3, s3, 0x1f400
	s_add_u32 s3, s12, s3
	s_addc_u32 s13, s13, s14
	s_mul_i32 s12, s6, 0x3e80
	s_add_u32 s12, s3, s12
	s_addc_u32 s3, s13, 0
	s_mov_b32 s11, 0x20000
	s_and_b32 s13, s3, 0xffff
	s_lshl_b32 s3, s6, 14
	s_and_b32 s7, s7, 12
	s_movk_i32 s14, 0x3e80
	s_mov_b32 s15, s11
	s_or_b32 s17, s7, s3
	s_lshl_b32 s3, s6, 7
	v_lshlrev_b32_e32 v36, 4, v0
	s_movk_i32 s6, 0x800
	buffer_load_dwordx4 v[30:33], v36, s[12:15], 0 offen
	buffer_load_dwordx4 v[26:29], v36, s[12:15], s6 offen
	s_movk_i32 s18, 0x1000
	s_movk_i32 s6, 0x1800
	buffer_load_dwordx4 v[22:25], v36, s[12:15], s18 offen
	buffer_load_dwordx4 v[18:21], v36, s[12:15], s6 offen
	s_movk_i32 s19, 0x2000
	s_movk_i32 s6, 0x2800
	s_movk_i32 s20, 0x3000
	buffer_load_dwordx4 v[14:17], v36, s[12:15], s19 offen
	buffer_load_dwordx4 v[10:13], v36, s[12:15], s6 offen
	s_movk_i32 s6, 0x3800
	buffer_load_dwordx4 v[6:9], v36, s[12:15], s20 offen
	buffer_load_dwordx4 v[2:5], v36, s[12:15], s6 offen
	v_and_b32_e32 v36, 15, v0
	v_or3_b32 v34, v34, s16, v36
	s_mov_b32 s10, 0x400000
	v_or_b32_e32 v35, s3, v0
	s_and_b32 s16, s2, 7
	s_lshl_b32 s16, s16, 14
	s_lshr_b32 s17, s2, 3
	s_lshl_b32 s17, s17, 9
	s_add_u32 s16, s16, s17
	v_lshl_add_u32 v34, v0, 2, s16
	s_mov_b32 s12, 0x40000
	s_and_b32 s5, s5, 0xffff
	s_mov_b32 s6, s11
	s_mov_b32 s7, s11
	v_lshlrev_b32_e32 v35, 2, v35
	s_mov_b32 s13, 0x60000
	s_mov_b32 s14, 0x80000
	s_mov_b32 s16, 0xa0000
	s_mov_b32 s21, 0xc0000
	s_mov_b32 s23, 0xe0000
	buffer_load_dword v40, v34, s[8:11], 0 offen
	buffer_load_dword v41, v34, s[8:11], s11 offen
	buffer_load_dword v42, v34, s[8:11], s12 offen
	buffer_load_dword v43, v34, s[8:11], s13 offen
	buffer_load_dword v44, v34, s[8:11], s14 offen
	buffer_load_dword v45, v34, s[8:11], s16 offen
	buffer_load_dword v46, v34, s[8:11], s21 offen
	buffer_load_dword v47, v34, s[8:11], s23 offen
	s_movk_i32 s12, 0x7000
	s_movk_i32 s15, 0x4000
	s_movk_i32 s17, 0x5000
	s_movk_i32 s22, 0x6000
	buffer_load_dword v48, v35, s[4:7], 0 offen
	buffer_load_dword v49, v35, s[4:7], s18 offen
	buffer_load_dword v50, v35, s[4:7], s19 offen
	buffer_load_dword v51, v35, s[4:7], s20 offen
	buffer_load_dword v52, v35, s[4:7], s15 offen
	buffer_load_dword v53, v35, s[4:7], s17 offen
	buffer_load_dword v54, v35, s[4:7], s22 offen
	buffer_load_dword v55, v35, s[4:7], s12 offen
	s_mov_b32 s12, 0x100000
	s_mov_b32 s13, 0x8000
	s_mov_b32 s14, 0x120000
	s_mov_b32 s16, 0x140000
	s_mov_b32 s18, 0x160000
	s_mov_b32 s20, 0x180000
	s_mov_b32 s22, 0x1a0000
	s_mov_b32 s24, 0x1c0000
	s_mov_b32 s26, 0x1e0000
	buffer_load_dword v56, v34, s[8:11], s12 offen
	buffer_load_dword v57, v34, s[8:11], s14 offen
	buffer_load_dword v58, v34, s[8:11], s16 offen
	buffer_load_dword v59, v34, s[8:11], s18 offen
	buffer_load_dword v60, v34, s[8:11], s20 offen
	buffer_load_dword v61, v34, s[8:11], s22 offen
	buffer_load_dword v62, v34, s[8:11], s24 offen
	buffer_load_dword v63, v34, s[8:11], s26 offen
	s_mov_b32 s12, 0xf000
	s_mov_b32 s15, 0x9000
	s_mov_b32 s17, 0xa000
	s_mov_b32 s19, 0xb000
	s_mov_b32 s21, 0xc000
	s_mov_b32 s23, 0xd000
	s_mov_b32 s25, 0xe000
	buffer_load_dword v64, v35, s[4:7], s13 offen
	buffer_load_dword v65, v35, s[4:7], s15 offen
	buffer_load_dword v66, v35, s[4:7], s17 offen
	buffer_load_dword v67, v35, s[4:7], s19 offen
	buffer_load_dword v68, v35, s[4:7], s21 offen
	buffer_load_dword v69, v35, s[4:7], s23 offen
	buffer_load_dword v70, v35, s[4:7], s25 offen
	buffer_load_dword v71, v35, s[4:7], s12 offen
	s_mov_b32 s12, 0x200000
	s_mov_b32 s13, 0x10000
	s_mov_b32 s14, 0x220000
	s_mov_b32 s16, 0x240000
	s_mov_b32 s18, 0x260000
	s_mov_b32 s20, 0x280000
	s_mov_b32 s22, 0x2a0000
	s_mov_b32 s24, 0x2c0000
	s_mov_b32 s26, 0x2e0000
	buffer_load_dword v72, v34, s[8:11], s12 offen
	buffer_load_dword v73, v34, s[8:11], s14 offen
	buffer_load_dword v74, v34, s[8:11], s16 offen
	buffer_load_dword v75, v34, s[8:11], s18 offen
	buffer_load_dword v76, v34, s[8:11], s20 offen
	buffer_load_dword v77, v34, s[8:11], s22 offen
	buffer_load_dword v78, v34, s[8:11], s24 offen
	buffer_load_dword v79, v34, s[8:11], s26 offen
	s_mov_b32 s12, 0x17000
	s_mov_b32 s15, 0x11000
	s_mov_b32 s17, 0x12000
	s_mov_b32 s19, 0x13000
	s_mov_b32 s21, 0x14000
	s_mov_b32 s23, 0x15000
	s_mov_b32 s25, 0x16000
	buffer_load_dword v80, v35, s[4:7], s13 offen
	buffer_load_dword v81, v35, s[4:7], s15 offen
	buffer_load_dword v82, v35, s[4:7], s17 offen
	buffer_load_dword v83, v35, s[4:7], s19 offen
	buffer_load_dword v84, v35, s[4:7], s21 offen
	buffer_load_dword v85, v35, s[4:7], s23 offen
	buffer_load_dword v86, v35, s[4:7], s25 offen
	buffer_load_dword v87, v35, s[4:7], s12 offen
	s_mov_b32 s12, 0x300000
	s_mov_b32 s13, 0x18000
	s_mov_b32 s14, 0x320000
	s_mov_b32 s15, 0x19000
	s_mov_b32 s16, 0x340000
	s_mov_b32 s17, 0x1a000
	s_mov_b32 s18, 0x360000
	s_mov_b32 s19, 0x1b000
	s_mov_b32 s20, 0x380000
	s_mov_b32 s21, 0x1c000
	s_mov_b32 s22, 0x3a0000
	s_mov_b32 s23, 0x1d000
	s_mov_b32 s24, 0x3c0000
	s_mov_b32 s25, 0x1e000
	s_mov_b32 s26, 0x3e0000
	buffer_load_dword v88, v34, s[8:11], s12 offen
	buffer_load_dword v89, v34, s[8:11], s14 offen
	buffer_load_dword v90, v34, s[8:11], s16 offen
	buffer_load_dword v91, v34, s[8:11], s18 offen
	buffer_load_dword v92, v34, s[8:11], s20 offen
	buffer_load_dword v93, v34, s[8:11], s22 offen
	buffer_load_dword v94, v34, s[8:11], s24 offen
	buffer_load_dword v95, v34, s[8:11], s26 offen
	s_mov_b32 s8, 0x1f000
	buffer_load_dword v96, v35, s[4:7], s13 offen
	buffer_load_dword v97, v35, s[4:7], s15 offen
	buffer_load_dword v98, v35, s[4:7], s17 offen
	buffer_load_dword v99, v35, s[4:7], s19 offen
	buffer_load_dword v100, v35, s[4:7], s21 offen
	buffer_load_dword v101, v35, s[4:7], s23 offen
	buffer_load_dword v102, v35, s[4:7], s25 offen
	buffer_load_dword v103, v35, s[4:7], s8 offen
	s_waitcnt vmcnt(62)
	v_cvt_f64_f32_e32 v[38:39], v27
	v_mul_f64 v[38:39], v[38:39], v[38:39]
	v_cvt_f64_f32_e32 v[26:27], v26
	v_fmac_f64_e32 v[38:39], v[26:27], v[26:27]
	v_cvt_f64_f32_e32 v[26:27], v28
	v_fmac_f64_e32 v[38:39], v[26:27], v[26:27]
	v_cvt_f64_f32_e32 v[26:27], v29
	v_fmac_f64_e32 v[38:39], v[26:27], v[26:27]
	v_cvt_f64_f32_e32 v[26:27], v23
	v_mul_f64 v[26:27], v[26:27], v[26:27]
	v_cvt_f64_f32_e32 v[22:23], v22
	v_fmac_f64_e32 v[26:27], v[22:23], v[22:23]
	v_cvt_f64_f32_e32 v[22:23], v24
	v_fmac_f64_e32 v[26:27], v[22:23], v[22:23]
	v_cvt_f64_f32_e32 v[22:23], v25
	v_fmac_f64_e32 v[26:27], v[22:23], v[22:23]
	v_cvt_f64_f32_e32 v[22:23], v19
	v_mul_f64 v[22:23], v[22:23], v[22:23]
	v_cvt_f64_f32_e32 v[18:19], v18
	v_fmac_f64_e32 v[22:23], v[18:19], v[18:19]
	v_cvt_f64_f32_e32 v[18:19], v20
	v_fmac_f64_e32 v[22:23], v[18:19], v[18:19]
	v_cvt_f64_f32_e32 v[18:19], v21
	v_fmac_f64_e32 v[22:23], v[18:19], v[18:19]
	v_cvt_f64_f32_e32 v[18:19], v15
	v_mul_f64 v[18:19], v[18:19], v[18:19]
	v_cvt_f64_f32_e32 v[14:15], v14
	v_fmac_f64_e32 v[18:19], v[14:15], v[14:15]
	v_cvt_f64_f32_e32 v[14:15], v16
	v_fmac_f64_e32 v[18:19], v[14:15], v[14:15]
	v_cvt_f64_f32_e32 v[14:15], v17
	v_fmac_f64_e32 v[18:19], v[14:15], v[14:15]
	v_cvt_f64_f32_e32 v[14:15], v11
	v_mul_f64 v[14:15], v[14:15], v[14:15]
	v_cvt_f64_f32_e32 v[10:11], v10
	v_fmac_f64_e32 v[14:15], v[10:11], v[10:11]
	v_cvt_f64_f32_e32 v[10:11], v12
	v_fmac_f64_e32 v[14:15], v[10:11], v[10:11]
	v_cvt_f64_f32_e32 v[10:11], v13
	v_fmac_f64_e32 v[14:15], v[10:11], v[10:11]
	v_cvt_f64_f32_e32 v[10:11], v7
	v_mul_f64 v[10:11], v[10:11], v[10:11]
	v_cvt_f64_f32_e32 v[6:7], v6
	v_fmac_f64_e32 v[10:11], v[6:7], v[6:7]
	v_cvt_f64_f32_e32 v[6:7], v8
	v_fmac_f64_e32 v[10:11], v[6:7], v[6:7]
	v_cvt_f64_f32_e32 v[6:7], v9
	v_fmac_f64_e32 v[10:11], v[6:7], v[6:7]
	v_cvt_f64_f32_e32 v[6:7], v3
	v_mul_f64 v[6:7], v[6:7], v[6:7]
	v_cvt_f64_f32_e32 v[2:3], v2
	v_fmac_f64_e32 v[6:7], v[2:3], v[2:3]
	v_cvt_f64_f32_e32 v[2:3], v4
	v_fmac_f64_e32 v[6:7], v[2:3], v[2:3]
	v_cvt_f64_f32_e32 v[2:3], v5
	v_fmac_f64_e32 v[6:7], v[2:3], v[2:3]
	v_cvt_f64_f32_e32 v[2:3], v40
	v_add_f64 v[2:3], v[2:3], 0
	s_waitcnt vmcnt(59)
	v_cvt_f64_f32_e32 v[4:5], v44
	v_add_f64 v[2:3], v[2:3], v[4:5]
	s_waitcnt vmcnt(55)
	v_cvt_f64_f32_e32 v[4:5], v48
	v_add_f64 v[4:5], v[4:5], 0
	s_waitcnt vmcnt(51)
	v_cvt_f64_f32_e32 v[8:9], v52
	v_add_f64 v[4:5], v[4:5], v[8:9]
	v_cvt_f64_f32_e32 v[8:9], v41
	v_add_f64 v[8:9], v[8:9], 0
	v_cvt_f64_f32_e32 v[12:13], v45
	v_add_f64 v[8:9], v[8:9], v[12:13]
	v_cvt_f64_f32_e32 v[12:13], v49
	v_add_f64 v[12:13], v[12:13], 0
	s_waitcnt vmcnt(50)
	v_cvt_f64_f32_e32 v[16:17], v53
	v_add_f64 v[12:13], v[12:13], v[16:17]
	v_cvt_f64_f32_e32 v[16:17], v42
	v_add_f64 v[16:17], v[16:17], 0
	v_cvt_f64_f32_e32 v[20:21], v46
	v_add_f64 v[16:17], v[16:17], v[20:21]
	v_cvt_f64_f32_e32 v[20:21], v50
	v_add_f64 v[20:21], v[20:21], 0
	s_waitcnt vmcnt(49)
	v_cvt_f64_f32_e32 v[24:25], v54
	v_add_f64 v[20:21], v[20:21], v[24:25]
	v_cvt_f64_f32_e32 v[24:25], v43
	v_add_f64 v[24:25], v[24:25], 0
	v_cvt_f64_f32_e32 v[28:29], v47
	v_add_f64 v[24:25], v[24:25], v[28:29]
	v_cvt_f64_f32_e32 v[28:29], v51
	v_add_f64 v[28:29], v[28:29], 0
	s_waitcnt vmcnt(48)
	v_cvt_f64_f32_e32 v[40:41], v55
	v_add_f64 v[28:29], v[28:29], v[40:41]
	s_waitcnt vmcnt(47)
	v_cvt_f64_f32_e32 v[40:41], v56
	v_add_f64 v[2:3], v[2:3], v[40:41]
	s_waitcnt vmcnt(39)
	v_cvt_f64_f32_e32 v[40:41], v64
	v_add_f64 v[4:5], v[4:5], v[40:41]
	v_cvt_f64_f32_e32 v[40:41], v57
	v_add_f64 v[8:9], v[8:9], v[40:41]
	s_waitcnt vmcnt(38)
	v_cvt_f64_f32_e32 v[40:41], v65
	v_add_f64 v[12:13], v[12:13], v[40:41]
	v_cvt_f64_f32_e32 v[40:41], v58
	v_add_f64 v[16:17], v[16:17], v[40:41]
	s_waitcnt vmcnt(37)
	v_cvt_f64_f32_e32 v[40:41], v66
	v_add_f64 v[20:21], v[20:21], v[40:41]
	v_cvt_f64_f32_e32 v[40:41], v59
	v_add_f64 v[24:25], v[24:25], v[40:41]
	s_waitcnt vmcnt(36)
	v_cvt_f64_f32_e32 v[40:41], v67
	v_add_f64 v[28:29], v[28:29], v[40:41]
	v_cvt_f64_f32_e32 v[40:41], v60
	v_add_f64 v[2:3], v[2:3], v[40:41]
	s_waitcnt vmcnt(35)
	v_cvt_f64_f32_e32 v[40:41], v68
	v_add_f64 v[4:5], v[4:5], v[40:41]
	v_cvt_f64_f32_e32 v[40:41], v61
	v_add_f64 v[8:9], v[8:9], v[40:41]
	s_waitcnt vmcnt(34)
	v_cvt_f64_f32_e32 v[40:41], v69
	v_add_f64 v[12:13], v[12:13], v[40:41]
	v_cvt_f64_f32_e32 v[40:41], v62
	v_add_f64 v[16:17], v[16:17], v[40:41]
	s_waitcnt vmcnt(33)
	v_cvt_f64_f32_e32 v[40:41], v70
	v_add_f64 v[20:21], v[20:21], v[40:41]
	v_cvt_f64_f32_e32 v[40:41], v63
	v_add_f64 v[24:25], v[24:25], v[40:41]
	s_waitcnt vmcnt(32)
	v_cvt_f64_f32_e32 v[40:41], v71
	v_add_f64 v[28:29], v[28:29], v[40:41]
	s_waitcnt vmcnt(31)
	v_cvt_f64_f32_e32 v[40:41], v72
	v_add_f64 v[2:3], v[2:3], v[40:41]
	s_waitcnt vmcnt(23)
	v_cvt_f64_f32_e32 v[40:41], v80
	v_add_f64 v[4:5], v[4:5], v[40:41]
	v_cvt_f64_f32_e32 v[40:41], v73
	v_add_f64 v[8:9], v[8:9], v[40:41]
	s_waitcnt vmcnt(22)
	v_cvt_f64_f32_e32 v[40:41], v81
	v_add_f64 v[12:13], v[12:13], v[40:41]
	v_cvt_f64_f32_e32 v[40:41], v74
	v_add_f64 v[16:17], v[16:17], v[40:41]
	s_waitcnt vmcnt(21)
	v_cvt_f64_f32_e32 v[40:41], v82
	v_add_f64 v[20:21], v[20:21], v[40:41]
	v_cvt_f64_f32_e32 v[40:41], v75
	v_add_f64 v[24:25], v[24:25], v[40:41]
	s_waitcnt vmcnt(20)
	v_cvt_f64_f32_e32 v[40:41], v83
	v_add_f64 v[28:29], v[28:29], v[40:41]
	v_cvt_f64_f32_e32 v[40:41], v76
	v_add_f64 v[2:3], v[2:3], v[40:41]
	s_waitcnt vmcnt(19)
	v_cvt_f64_f32_e32 v[40:41], v84
	v_add_f64 v[4:5], v[4:5], v[40:41]
	v_cvt_f64_f32_e32 v[40:41], v77
	v_add_f64 v[8:9], v[8:9], v[40:41]
	s_waitcnt vmcnt(18)
	v_cvt_f64_f32_e32 v[40:41], v85
	v_add_f64 v[12:13], v[12:13], v[40:41]
	v_cvt_f64_f32_e32 v[40:41], v78
	v_add_f64 v[16:17], v[16:17], v[40:41]
	s_waitcnt vmcnt(17)
	v_cvt_f64_f32_e32 v[40:41], v86
	v_add_f64 v[20:21], v[20:21], v[40:41]
	v_cvt_f64_f32_e32 v[40:41], v79
	v_add_f64 v[24:25], v[24:25], v[40:41]
	s_waitcnt vmcnt(16)
	v_cvt_f64_f32_e32 v[40:41], v87
	v_add_f64 v[28:29], v[28:29], v[40:41]
	s_waitcnt vmcnt(15)
	v_cvt_f64_f32_e32 v[40:41], v88
	v_add_f64 v[2:3], v[2:3], v[40:41]
	s_waitcnt vmcnt(7)
	v_cvt_f64_f32_e32 v[40:41], v96
	v_add_f64 v[4:5], v[4:5], v[40:41]
	v_cvt_f64_f32_e32 v[40:41], v89
	v_add_f64 v[8:9], v[8:9], v[40:41]
	s_waitcnt vmcnt(6)
	v_cvt_f64_f32_e32 v[40:41], v97
	v_add_f64 v[12:13], v[12:13], v[40:41]
	v_cvt_f64_f32_e32 v[40:41], v90
	v_add_f64 v[16:17], v[16:17], v[40:41]
	s_waitcnt vmcnt(5)
	v_cvt_f64_f32_e32 v[40:41], v98
	v_add_f64 v[20:21], v[20:21], v[40:41]
	v_cvt_f64_f32_e32 v[40:41], v91
	v_add_f64 v[24:25], v[24:25], v[40:41]
	s_waitcnt vmcnt(4)
	v_cvt_f64_f32_e32 v[40:41], v99
	v_add_f64 v[28:29], v[28:29], v[40:41]
	v_cvt_f64_f32_e32 v[40:41], v92
	v_add_f64 v[2:3], v[2:3], v[40:41]
	s_waitcnt vmcnt(3)
	v_cvt_f64_f32_e32 v[40:41], v100
	v_add_f64 v[4:5], v[4:5], v[40:41]
	v_cvt_f64_f32_e32 v[40:41], v93
	v_add_f64 v[8:9], v[8:9], v[40:41]
	s_waitcnt vmcnt(2)
	v_cvt_f64_f32_e32 v[40:41], v101
	v_add_f64 v[12:13], v[12:13], v[40:41]
	v_cvt_f64_f32_e32 v[40:41], v94
	v_add_f64 v[16:17], v[16:17], v[40:41]
	s_waitcnt vmcnt(1)
	v_cvt_f64_f32_e32 v[40:41], v102
	v_add_f64 v[20:21], v[20:21], v[40:41]
	v_cvt_f64_f32_e32 v[40:41], v95
	v_add_f64 v[24:25], v[24:25], v[40:41]
	s_waitcnt vmcnt(0)
	v_cvt_f64_f32_e32 v[40:41], v103
	v_add_f64 v[28:29], v[28:29], v[40:41]
	v_add_f64 v[2:3], v[2:3], v[8:9]
	v_add_f64 v[8:9], v[16:17], v[24:25]
	v_add_f64 v[2:3], v[2:3], v[8:9]
	v_add_f64 v[4:5], v[4:5], v[12:13]
	v_add_f64 v[8:9], v[20:21], v[28:29]
	v_add_f64 v[4:5], v[4:5], v[8:9]
	s_mov_b32 s4, 0
	v_fmac_f64_e32 v[4:5], -2.0, v[2:3]
	s_mov_b32 s5, 0xc0df4000
	v_add_f64 v[2:3], v[4:5], s[4:5]
	v_cvt_f32_f64_e32 v3, v[2:3]
	v_cvt_f64_f32_e32 v[34:35], v30
	v_cvt_f64_f32_e32 v[30:31], v31
	v_mov_b32_dpp v2, v3 quad_perm:[1,0,3,2] row_mask:0xf bank_mask:0xf bound_ctrl:1
	v_max_f32_e32 v2, v2, v2
	v_min_f32_e32 v2, v3, v2
	v_mul_f64 v[30:31], v[30:31], v[30:31]
	v_cvt_f64_f32_e32 v[36:37], v32
	v_mov_b32_dpp v4, v2 quad_perm:[2,3,0,1] row_mask:0xf bank_mask:0xf bound_ctrl:1
	v_max_f32_e32 v4, v4, v4
	v_min_f32_e32 v2, v2, v4
	v_fmac_f64_e32 v[30:31], v[34:35], v[34:35]
	v_cvt_f64_f32_e32 v[32:33], v33
	v_mov_b32_dpp v4, v2 row_half_mirror row_mask:0xf bank_mask:0xf bound_ctrl:1
	v_fmac_f64_e32 v[30:31], v[36:37], v[36:37]
	v_max_f32_e32 v4, v4, v4
	v_fmac_f64_e32 v[30:31], v[32:33], v[32:33]
	v_min_f32_e32 v2, v2, v4
	v_add_f64 v[30:31], v[30:31], v[38:39]
	v_add_f64 v[26:27], v[30:31], v[26:27]
	v_mov_b32_dpp v4, v2 row_mirror row_mask:0xf bank_mask:0xf bound_ctrl:1
	v_max_f32_e32 v4, v4, v4
	v_add_f64 v[22:23], v[26:27], v[22:23]
	v_min_f32_e32 v2, v2, v4
	v_add_f64 v[18:19], v[22:23], v[18:19]
	v_readlane_b32 s6, v2, 32
	v_readlane_b32 s7, v2, 48
	v_add_f64 v[14:15], v[18:19], v[14:15]
	v_readlane_b32 s4, v2, 0
	v_readlane_b32 s5, v2, 16
	v_max_f32_e64 v2, s7, s7
	v_max_f32_e64 v4, s6, s6
	v_add_f64 v[10:11], v[14:15], v[10:11]
	v_min_f32_e32 v2, v4, v2
	v_mov_b32_e32 v4, s5
	v_add_f64 v[6:7], v[10:11], v[6:7]
	v_min3_f32 v2, s4, v4, v2
	v_cmp_eq_f32_e32 vcc, v2, v3
	v_cvt_f32_f64_e32 v3, v[6:7]
	s_nop 1
	v_add_f32_dpp v3, v3, v3 quad_perm:[1,0,3,2] row_mask:0xf bank_mask:0xf bound_ctrl:1
	s_nop 1
	v_add_f32_dpp v3, v3, v3 quad_perm:[2,3,0,1] row_mask:0xf bank_mask:0xf bound_ctrl:1
	s_nop 1
	v_add_f32_dpp v3, v3, v3 row_half_mirror row_mask:0xf bank_mask:0xf bound_ctrl:1
	s_nop 1
	v_add_f32_dpp v3, v3, v3 row_mirror row_mask:0xf bank_mask:0xf bound_ctrl:1
	s_nop 0
	v_readlane_b32 s8, v3, 0
	v_readlane_b32 s10, v3, 16
	v_readlane_b32 s9, v3, 32
	v_readlane_b32 s11, v3, 48
	v_and_b32_e32 v3, 63, v0
	v_cmp_eq_u32_e64 s[4:5], 0, v3
	s_and_saveexec_b64 s[6:7], s[4:5]
	s_cbranch_execz .LBB1_2
	v_mov_b32_e32 v4, s10
	v_mov_b32_e32 v5, s11
	s_ff1_i32_b64 s4, vcc
	v_pk_add_f32 v[4:5], s[8:9], v[4:5]
	v_and_or_b32 v3, v0, 64, s4
	v_add_f32_e32 v4, v4, v5
	v_or_b32_e32 v5, s3, v3
	v_lshrrev_b32_e32 v6, 4, v0
	v_cvt_f64_f32_e32 v[2:3], v2
	ds_write_b32 v6, v5 offset:32
	v_cvt_f64_f32_e32 v[4:5], v4
	ds_write2_b64 v1, v[2:3], v[4:5] offset1:2
